# baseline (speedup 1.0000x reference)
.LBB1_99:
	s_or_b64 exec, exec, s[0:1]
	s_lshl_b32 s0, s30, 8
	s_add_i32 s0, s0, s2
	s_mov_b32 s1, s31
	s_lshl_b64 s[4:5], s[0:1], 9
	s_cmpk_lt_u32 s0, 0x1f40
	s_cselect_b64 s[0:1], -1, 0
	v_lshlrev_b32_e32 v98, 1, v179
	v_and_b32_e32 v98, 0x1fe, v98
	s_and_b64 s[0:1], s[68:69], s[0:1]
	v_or_b32_e32 v100, s4, v98
	v_cndmask_b32_e64 v98, 0, 1, s[0:1]
	v_mov_b32_e32 v101, s5
	v_cmp_ne_u32_e64 s[4:5], 1, v98
	s_andn2_b64 vcc, exec, s[0:1]
	s_cbranch_vccnz .LBB1_101
	v_lshlrev_b64 v[246:247], 5, v[100:101]
	v_lshl_add_u64 v[246:247], s[64:65], 0, v[246:247]
	global_load_dwordx4 v[180:183], v[246:247], off
	global_load_dwordx4 v[184:187], v[246:247], off offset:16
	global_load_dwordx4 v[188:191], v[246:247], off offset:32
	global_load_dwordx4 v[242:245], v[246:247], off offset:48

.LBB1_115:
	s_or_b64 exec, exec, s[0:1]
	s_and_b64 vcc, exec, s[4:5]
	s_cbranch_vccnz .LBB1_117
	v_cvt_pk_f16_f32 v104, v180, v181
	v_cvt_pk_f16_f32 v105, v182, v183
	v_cvt_pk_f16_f32 v106, v184, v185
	v_cvt_pk_f16_f32 v107, v186, v187
	v_cvt_pk_f16_f32 v110, v188, v189
	v_cvt_pk_f16_f32 v111, v190, v191
	v_cvt_pk_f16_f32 v112, v242, v243
	v_cvt_pk_f16_f32 v113, v244, v245
	v_lshl_add_u64 v[100:101], v[100:101], 4, s[66:67]
	global_store_dwordx4 v[100:101], v[104:107], off
	global_store_dwordx4 v[100:101], v[110:113], off offset:16

	.amdhsa_kernel _Z9k_persist11PersistArgs
		.amdhsa_group_segment_fixed_size 0
		.amdhsa_private_segment_fixed_size 0
		.amdhsa_kernarg_size 192
		.amdhsa_user_sgpr_count 2
		.amdhsa_user_sgpr_dispatch_ptr 0
		.amdhsa_user_sgpr_queue_ptr 0
		.amdhsa_user_sgpr_kernarg_segment_ptr 1
		.amdhsa_user_sgpr_dispatch_id 0
		.amdhsa_user_sgpr_kernarg_preload_length 0
		.amdhsa_user_sgpr_kernarg_preload_offset 0
		.amdhsa_user_sgpr_private_segment_size 0
		.amdhsa_uses_dynamic_stack 0
		.amdhsa_enable_private_segment 0
		.amdhsa_system_sgpr_workgroup_id_x 1
		.amdhsa_system_sgpr_workgroup_id_y 0
		.amdhsa_system_sgpr_workgroup_id_z 0
		.amdhsa_system_sgpr_workgroup_info 0
		.amdhsa_system_vgpr_workitem_id 0
		.amdhsa_next_free_vgpr 248
		.amdhsa_next_free_sgpr 100
		.amdhsa_accum_offset 248
		.amdhsa_reserve_vcc 1
		.amdhsa_float_round_mode_32 0
		.amdhsa_float_round_mode_16_64 0
		.amdhsa_float_denorm_mode_32 3
		.amdhsa_float_denorm_mode_16_64 3
		.amdhsa_dx10_clamp 1
		.amdhsa_ieee_mode 1
		.amdhsa_fp16_overflow 0
		.amdhsa_tg_split 0
		.amdhsa_exception_fp_ieee_invalid_op 0
		.amdhsa_exception_fp_denorm_src 0
		.amdhsa_exception_fp_ieee_div_zero 0
		.amdhsa_exception_fp_ieee_overflow 0
		.amdhsa_exception_fp_ieee_underflow 0
		.amdhsa_exception_fp_ieee_inexact 0
		.amdhsa_exception_int_div_zero 0
	.end_amdhsa_kernel

amdhsa.kernels:
  - .agpr_count:     0
    .args:
      - .offset:         0
        .size:           200
        .value_kind:     by_value
    .group_segment_fixed_size: 4224
    .kernarg_segment_align: 8
    .kernarg_segment_size: 200
    .language:       OpenCL C
    .language_version:
      - 2
      - 0
    .max_flat_workgroup_size: 256
    .name:           _Z10k_prep_all8PrepArgs
    .private_segment_fixed_size: 0
    .sgpr_count:     74
    .sgpr_spill_count: 0
    .symbol:         _Z10k_prep_all8PrepArgs.kd
    .uniform_work_group_size: 1
    .uses_dynamic_stack: false
    .vgpr_count:     27
    .vgpr_spill_count: 0
    .wavefront_size: 64
  - .agpr_count:     0
    .args:
      - .offset:         0
        .size:           192
        .value_kind:     by_value
    .group_segment_fixed_size: 0
    .kernarg_segment_align: 8
    .kernarg_segment_size: 192
    .language:       OpenCL C
    .language_version:
      - 2
      - 0
    .max_flat_workgroup_size: 512
    .name:           _Z9k_persist11PersistArgs
    .private_segment_fixed_size: 0
    .sgpr_count:     106
    .sgpr_spill_count: 32
    .symbol:         _Z9k_persist11PersistArgs.kd
    .uniform_work_group_size: 1
    .uses_dynamic_stack: false
    .vgpr_count:     248
    .vgpr_spill_count: 0
    .wavefront_size: 64
  - .agpr_count:     0
    .args:
      - .actual_access:  read_only
        .address_space:  global
        .offset:         0
        .size:           8
        .value_kind:     global_buffer
      - .actual_access:  write_only
        .address_space:  global
        .offset:         8
        .size:           8
        .value_kind:     global_buffer
    .group_segment_fixed_size: 32
    .kernarg_segment_align: 8
    .kernarg_segment_size: 16
    .language:       OpenCL C
    .language_version:
      - 2
      - 0
    .max_flat_workgroup_size: 256
    .name:           _Z11k_lse_finalPKDF16_Pf
    .private_segment_fixed_size: 0
    .sgpr_count:     20
    .sgpr_spill_count: 0
    .symbol:         _Z11k_lse_finalPKDF16_Pf.kd
    .uniform_work_group_size: 1
    .uses_dynamic_stack: false
    .vgpr_count:     148
    .vgpr_spill_count: 0
    .wavefront_size: 64
  - .agpr_count:     0
    .args:
      - .address_space:  global
        .offset:         0
        .size:           8
        .value_kind:     global_buffer
      - .address_space:  global
        .offset:         8
        .size:           8
        .value_kind:     global_buffer
      - .actual_access:  write_only
        .address_space:  global
        .offset:         16
        .size:           8
        .value_kind:     global_buffer
      - .actual_access:  read_only
        .address_space:  global
        .offset:         24
        .size:           8
        .value_kind:     global_buffer
      - .actual_access:  read_only
        .address_space:  global
        .offset:         32
        .size:           8
        .value_kind:     global_buffer
      - .actual_access:  read_only
        .address_space:  global
        .offset:         40
        .size:           8
        .value_kind:     global_buffer
      - .offset:         48
        .size:           4
        .value_kind:     by_value
      - .offset:         52
        .size:           4
        .value_kind:     by_value
      - .actual_access:  read_only
        .address_space:  global
        .offset:         56
        .size:           8
        .value_kind:     global_buffer
      - .actual_access:  read_only
        .address_space:  global
        .offset:         64
        .size:           8
        .value_kind:     global_buffer
      - .actual_access:  read_only
        .address_space:  global
        .offset:         72
        .size:           8
        .value_kind:     global_buffer
    .group_segment_fixed_size: 0
    .kernarg_segment_align: 8
    .kernarg_segment_size: 80
    .language:       OpenCL C
    .language_version:
      - 2
      - 0
    .max_flat_workgroup_size: 512
    .name:           _Z6k_gemmILi8ELi512ELi0ELb0ELi0EEvPKDF16_S1_PfPDF16_S3_PKfiiS1_S1_S3_
    .private_segment_fixed_size: 0
    .sgpr_count:     32
    .sgpr_spill_count: 0
    .symbol:         _Z6k_gemmILi8ELi512ELi0ELb0ELi0EEvPKDF16_S1_PfPDF16_S3_PKfiiS1_S1_S3_.kd
    .uniform_work_group_size: 1
    .uses_dynamic_stack: false
    .vgpr_count:     246
    .vgpr_spill_count: 0
    .wavefront_size: 64
  - .agpr_count:     0
    .args:
      - .address_space:  global
        .offset:         0
        .size:           8
        .value_kind:     global_buffer
      - .address_space:  global
        .offset:         8
        .size:           8
        .value_kind:     global_buffer
      - .actual_access:  read_only
        .address_space:  global
        .offset:         16
        .size:           8
        .value_kind:     global_buffer
      - .actual_access:  write_only
        .address_space:  global
        .offset:         24
        .size:           8
        .value_kind:     global_buffer
      - .actual_access:  read_only
        .address_space:  global
        .offset:         32
        .size:           8
        .value_kind:     global_buffer
      - .actual_access:  read_only
        .address_space:  global
        .offset:         40
        .size:           8
        .value_kind:     global_buffer
      - .offset:         48
        .size:           4
        .value_kind:     by_value
      - .offset:         52
        .size:           4
        .value_kind:     by_value
      - .actual_access:  read_only
        .address_space:  global
        .offset:         56
        .size:           8
        .value_kind:     global_buffer
      - .actual_access:  read_only
        .address_space:  global
        .offset:         64
        .size:           8
        .value_kind:     global_buffer
      - .actual_access:  read_only
        .address_space:  global
        .offset:         72
        .size:           8
        .value_kind:     global_buffer
    .group_segment_fixed_size: 0
    .kernarg_segment_align: 8
    .kernarg_segment_size: 80
    .language:       OpenCL C
    .language_version:
      - 2
      - 0
    .max_flat_workgroup_size: 512
    .name:           _Z6k_gemmILi16ELi1024ELi0ELb0ELi3EEvPKDF16_S1_PfPDF16_S3_PKfiiS1_S1_S3_
    .private_segment_fixed_size: 0
    .sgpr_count:     36
    .sgpr_spill_count: 0
    .symbol:         _Z6k_gemmILi16ELi1024ELi0ELb0ELi3EEvPKDF16_S1_PfPDF16_S3_PKfiiS1_S1_S3_.kd
    .uniform_work_group_size: 1
    .uses_dynamic_stack: false
    .vgpr_count:     246
    .vgpr_spill_count: 0
    .wavefront_size: 64
  - .agpr_count:     0
    .args:
      - .address_space:  global
        .offset:         0
        .size:           8
        .value_kind:     global_buffer
      - .address_space:  global
        .offset:         8
        .size:           8
        .value_kind:     global_buffer
      - .actual_access:  read_only
        .address_space:  global
        .offset:         16
        .size:           8
        .value_kind:     global_buffer
      - .actual_access:  write_only
        .address_space:  global
        .offset:         24
        .size:           8
        .value_kind:     global_buffer
      - .actual_access:  write_only
        .address_space:  global
        .offset:         32
        .size:           8
        .value_kind:     global_buffer
      - .actual_access:  read_only
        .address_space:  global
        .offset:         40
        .size:           8
        .value_kind:     global_buffer
      - .offset:         48
        .size:           4
        .value_kind:     by_value
      - .offset:         52
        .size:           4
        .value_kind:     by_value
      - .address_space:  global
        .offset:         56
        .size:           8
        .value_kind:     global_buffer
      - .address_space:  global
        .offset:         64
        .size:           8
        .value_kind:     global_buffer
      - .actual_access:  write_only
        .address_space:  global
        .offset:         72
        .size:           8
        .value_kind:     global_buffer
    .group_segment_fixed_size: 0
    .kernarg_segment_align: 8
    .kernarg_segment_size: 80
    .language:       OpenCL C
    .language_version:
      - 2
      - 0
    .max_flat_workgroup_size: 512
    .name:           _Z6k_gemmILi48ELi2048ELi1ELb1ELi12EEvPKDF16_S1_PfPDF16_S3_PKfiiS1_S1_S3_
    .private_segment_fixed_size: 0
    .sgpr_count:     26
    .sgpr_spill_count: 0
    .symbol:         _Z6k_gemmILi48ELi2048ELi1ELb1ELi12EEvPKDF16_S1_PfPDF16_S3_PKfiiS1_S1_S3_.kd
    .uniform_work_group_size: 1
    .uses_dynamic_stack: false
    .vgpr_count:     242
    .vgpr_spill_count: 0
    .wavefront_size: 64
